# combo8 + GEMM K-loops: first iteration peeled with srcC=0, the 62 v_mov_b64 accumulator zeroing per tile removed (all four GEMMs)
# speedup vs baseline: 1.0049x; 1.0049x over previous
.LBB0_243:
	s_add_u32 s22, s22, 0x20080
	s_addc_u32 s23, s23, 0
	s_add_u32 s17, s24, 0x100
	v_mov_b32_e32 v183, 0x1200
	s_addc_u32 s19, s25, 0
	s_mov_b32 s28, -2
	ds_read_b128 v[138:141], v134
	ds_read_b128 v[146:149], v134 offset:2048
	ds_read_b128 v[142:145], v135
	ds_read_b128 v[150:153], v135 offset:2048
	ds_read_b128 v[154:157], v134 offset:16384
	ds_read_b128 v[162:165], v134 offset:18432
	ds_read_b128 v[158:161], v135 offset:16384
	ds_read_b128 v[166:169], v135 offset:18432
	s_add_u32 s24, s22, 0xfffe0080
	s_addc_u32 s25, s23, -1
	s_cmp_eq_u32 s28, 4
	s_cselect_b32 s25, s5, s25
	s_cselect_b32 s24, s4, s24
	s_cselect_b32 s27, s21, s19
	s_cselect_b32 s26, s20, s17
	v_mov_b32_e32 v128, v136
	ds_read_b128 v[170:173], v132
	ds_read_b128 v[194:197], v132 offset:2048
	ds_read_b128 v[174:177], v133
	ds_read_b128 v[198:201], v133 offset:2048
	ds_read_b128 v[228:231], v132 offset:4096
	ds_read_b128 v[236:239], v132 offset:6144
	ds_read_b128 v[232:235], v133 offset:4096
	ds_read_b128 v[240:243], v133 offset:6144
	s_add_i32 m0, s30, 0xc000
	s_nop 0
	global_load_lds_dwordx4 v128, s[22:23]
	v_mov_b32_e32 v128, v137
	s_add_i32 m0, s30, 0xe000
	s_nop 0
	global_load_lds_dwordx4 v128, s[22:23]
	s_waitcnt vmcnt(8)
	s_waitcnt lgkmcnt(0)
	s_barrier
	s_setprio 1
	s_waitcnt lgkmcnt(0)
	v_mfma_f32_16x16x128_f8f6f4 v[124:127], v[138:145], v[170:177], 0
	v_mfma_f32_16x16x128_f8f6f4 v[120:123], v[146:153], v[170:177], 0
	v_mfma_f32_16x16x128_f8f6f4 v[108:111], v[138:145], v[194:201], 0
	v_mfma_f32_16x16x128_f8f6f4 v[104:107], v[146:153], v[194:201], 0
	v_mfma_f32_16x16x128_f8f6f4 v[128:131], v[138:145], v[228:235], 0
	v_mfma_f32_16x16x128_f8f6f4 v[178:181], v[146:153], v[228:235], 0
	v_mfma_f32_16x16x128_f8f6f4 v[202:205], v[138:145], v[236:243], 0
	v_mfma_f32_16x16x128_f8f6f4 v[244:247], v[146:153], v[236:243], 0
	s_setprio 0
	s_setprio 1
	v_mfma_f32_16x16x128_f8f6f4 v[116:119], v[154:161], v[170:177], 0
	v_mfma_f32_16x16x128_f8f6f4 v[112:115], v[162:169], v[170:177], 0
	v_mfma_f32_16x16x128_f8f6f4 v[100:103], v[154:161], v[194:201], 0
	v_mfma_f32_16x16x128_f8f6f4 v[96:99], v[162:169], v[194:201], 0
	v_mfma_f32_16x16x128_f8f6f4 v[170:173], v[154:161], v[228:235], 0
	v_mfma_f32_16x16x128_f8f6f4 v[174:177], v[162:169], v[228:235], 0
	v_mfma_f32_16x16x128_f8f6f4 v[194:197], v[154:161], v[236:243], 0
	v_mfma_f32_16x16x128_f8f6f4 v[198:201], v[162:169], v[236:243], 0
	s_setprio 0
	s_barrier
	v_mov_b32_e32 v182, v136
	s_mov_b32 m0, s31
	s_nop 2
	ds_read_b128 v[64:67], v132 offset:16384
	ds_read_b128 v[72:75], v132 offset:18432
	ds_read_b128 v[68:71], v133 offset:16384
	ds_read_b128 v[76:79], v133 offset:18432
	ds_read_b128 v[80:83], v132 offset:20480
	ds_read_b128 v[88:91], v132 offset:22528
	ds_read_b128 v[84:87], v133 offset:20480
	ds_read_b128 v[92:95], v133 offset:22528
	s_add_u32 s64, s26, 0x20000
	global_load_lds_dwordx4 v182, s[26:27]
	v_mov_b32_e32 v182, v137
	s_mov_b32 m0, s33
	s_addc_u32 s65, s27, 0
	global_load_lds_dwordx4 v182, s[26:27]
	v_mov_b32_e32 v182, v136
	s_mov_b32 m0, s34
	s_nop 0
	global_load_lds_dwordx4 v182, s[64:65]
	v_mov_b32_e32 v182, v137
	s_mov_b32 m0, s35
	s_nop 0
	global_load_lds_dwordx4 v182, s[64:65]
	v_mov_b32_e32 v182, v136
	s_mov_b32 m0, s30
	s_nop 0
	global_load_lds_dwordx4 v182, s[24:25]
	v_mov_b32_e32 v182, v137
	s_mov_b32 m0, s36
	s_nop 0
	global_load_lds_dwordx4 v182, s[24:25]
	s_waitcnt vmcnt(8)
	s_waitcnt lgkmcnt(0)
	s_barrier
	s_setprio 1
	s_waitcnt lgkmcnt(0)
	v_mfma_f32_16x16x128_f8f6f4 v[60:63], v[138:145], v[64:71], 0
	v_mfma_f32_16x16x128_f8f6f4 v[56:59], v[146:153], v[64:71], 0
	v_mfma_f32_16x16x128_f8f6f4 v[228:231], v[138:145], v[72:79], 0
	v_mfma_f32_16x16x128_f8f6f4 v[232:235], v[146:153], v[72:79], 0
	v_mfma_f32_16x16x128_f8f6f4 v[236:239], v[138:145], v[80:87], 0
	v_mfma_f32_16x16x128_f8f6f4 v[240:243], v[146:153], v[80:87], 0
	v_mfma_f32_16x16x128_f8f6f4 v[248:251], v[138:145], v[88:95], 0
	v_mfma_f32_16x16x128_f8f6f4 v[186:189], v[146:153], v[88:95], 0
	s_setprio 0
	s_setprio 1
	v_mfma_f32_16x16x128_f8f6f4 v[52:55], v[154:161], v[64:71], 0
	v_mfma_f32_16x16x128_f8f6f4 v[48:51], v[162:169], v[64:71], 0
	v_mfma_f32_16x16x128_f8f6f4 v[190:193], v[154:161], v[72:79], 0
	v_mfma_f32_16x16x128_f8f6f4 v[210:213], v[162:169], v[72:79], 0
	v_mfma_f32_16x16x128_f8f6f4 v[206:209], v[154:161], v[80:87], 0
	v_mfma_f32_16x16x128_f8f6f4 v[214:217], v[162:169], v[80:87], 0
	v_mfma_f32_16x16x128_f8f6f4 v[222:225], v[154:161], v[88:95], 0
	v_mfma_f32_16x16x128_f8f6f4 v[218:221], v[162:169], v[88:95], 0
	s_setprio 0
	s_barrier
	s_nop 4
	ds_read_b128 v[0:3], v134 offset:32768
	ds_read_b128 v[16:19], v134 offset:34816
	ds_read_b128 v[4:7], v135 offset:32768
	ds_read_b128 v[20:23], v135 offset:34816
	ds_read_b128 v[138:141], v134 offset:49152
	ds_read_b128 v[146:149], v134 offset:51200
	ds_read_b128 v[142:145], v135 offset:49152
	ds_read_b128 v[150:153], v135 offset:51200
	s_add_u32 s64, s24, 0x20000
	v_mov_b32_e32 v64, v136
	s_mov_b32 m0, s37
	ds_read_b128 v[8:11], v132 offset:32768
	ds_read_b128 v[24:27], v132 offset:34816
	ds_read_b128 v[12:15], v133 offset:32768
	ds_read_b128 v[28:31], v133 offset:34816
	ds_read_b128 v[32:35], v132 offset:36864
	ds_read_b128 v[40:43], v132 offset:38912
	ds_read_b128 v[36:39], v133 offset:36864
	ds_read_b128 v[44:47], v133 offset:38912
	s_addc_u32 s65, s25, 0
	s_nop 0
	global_load_lds_dwordx4 v64, s[64:65]
	v_mov_b32_e32 v64, v137
	s_mov_b32 m0, s38
	s_nop 0
	global_load_lds_dwordx4 v64, s[64:65]
	s_waitcnt vmcnt(8)
	s_waitcnt lgkmcnt(0)
	s_barrier
	s_setprio 1
	s_waitcnt lgkmcnt(0)
	v_mfma_f32_16x16x128_f8f6f4 v[124:127], v[0:7], v[8:15], v[124:127]
	v_mfma_f32_16x16x128_f8f6f4 v[120:123], v[16:23], v[8:15], v[120:123]
	v_mfma_f32_16x16x128_f8f6f4 v[108:111], v[0:7], v[24:31], v[108:111]
	v_mfma_f32_16x16x128_f8f6f4 v[104:107], v[16:23], v[24:31], v[104:107]
	v_mfma_f32_16x16x128_f8f6f4 v[92:95], v[0:7], v[32:39], v[128:131]
	v_mfma_f32_16x16x128_f8f6f4 v[88:91], v[16:23], v[32:39], v[178:181]
	v_mfma_f32_16x16x128_f8f6f4 v[76:79], v[0:7], v[40:47], v[202:205]
	v_mfma_f32_16x16x128_f8f6f4 v[72:75], v[16:23], v[40:47], v[244:247]
	s_setprio 0
	s_setprio 1
	v_mfma_f32_16x16x128_f8f6f4 v[116:119], v[138:145], v[8:15], v[116:119]
	v_mfma_f32_16x16x128_f8f6f4 v[112:115], v[146:153], v[8:15], v[112:115]
	v_mfma_f32_16x16x128_f8f6f4 v[100:103], v[138:145], v[24:31], v[100:103]
	v_mfma_f32_16x16x128_f8f6f4 v[96:99], v[146:153], v[24:31], v[96:99]
	v_mfma_f32_16x16x128_f8f6f4 v[84:87], v[138:145], v[32:39], v[170:173]
	v_mfma_f32_16x16x128_f8f6f4 v[80:83], v[146:153], v[32:39], v[174:177]
	v_mfma_f32_16x16x128_f8f6f4 v[68:71], v[138:145], v[40:47], v[194:197]
	v_mfma_f32_16x16x128_f8f6f4 v[64:67], v[146:153], v[40:47], v[198:201]
	s_setprio 0
	s_barrier
	v_mov_b32_e32 v184, v136
	ds_read_b128 v[32:35], v132 offset:49152
	ds_read_b128 v[154:157], v132 offset:51200
	ds_read_b128 v[36:39], v133 offset:49152
	ds_read_b128 v[158:161], v133 offset:51200
	ds_read_b128 v[162:165], v132 offset:53248
	ds_read_b128 v[170:173], v132 offset:55296
	ds_read_b128 v[166:169], v133 offset:53248
	ds_read_b128 v[174:177], v133 offset:55296
	s_mov_b32 m0, s42
	v_lshl_add_u64 v[8:9], s[26:27], 0, v[184:185]
	v_lshl_add_u64 v[8:9], v[8:9], 0, s[46:47]
	v_mov_b32_e32 v184, v137
	global_load_lds_dwordx4 v[8:9], off
	s_mov_b32 m0, s43
	v_lshl_add_u64 v[8:9], s[26:27], 0, v[184:185]
	v_lshl_add_u64 v[8:9], v[8:9], 0, s[46:47]
	global_load_lds_dwordx4 v[8:9], off
	s_add_u32 s26, s26, 0x20080
	v_mov_b32_e32 v8, v136
	s_addc_u32 s27, s27, 0
	s_mov_b32 m0, s50
	v_mov_b32_e32 v184, v136
	global_load_lds_dwordx4 v8, s[26:27]
	v_mov_b32_e32 v8, v137
	s_mov_b32 m0, s51
	s_nop 0
	global_load_lds_dwordx4 v8, s[26:27]
	s_mov_b32 m0, s44
	v_lshl_add_u64 v[8:9], s[24:25], 0, v[184:185]
	v_lshl_add_u64 v[8:9], v[8:9], 0, s[46:47]
	v_mov_b32_e32 v184, v137
	global_load_lds_dwordx4 v[8:9], off
	s_mov_b32 m0, s49
	v_lshl_add_u64 v[8:9], s[24:25], 0, v[184:185]
	v_lshl_add_u64 v[8:9], v[8:9], 0, s[46:47]
	global_load_lds_dwordx4 v[8:9], off
	s_waitcnt vmcnt(8)
	s_waitcnt lgkmcnt(0)
	s_barrier
	s_setprio 1
	s_waitcnt lgkmcnt(0)
	v_mfma_f32_16x16x128_f8f6f4 v[60:63], v[0:7], v[32:39], v[60:63]
	v_mfma_f32_16x16x128_f8f6f4 v[56:59], v[16:23], v[32:39], v[56:59]
	v_mfma_f32_16x16x128_f8f6f4 v[44:47], v[0:7], v[154:161], v[228:231]
	v_mfma_f32_16x16x128_f8f6f4 v[40:43], v[16:23], v[154:161], v[232:235]
	v_mfma_f32_16x16x128_f8f6f4 v[28:31], v[0:7], v[162:169], v[236:239]
	v_mfma_f32_16x16x128_f8f6f4 v[24:27], v[16:23], v[162:169], v[240:243]
	v_mfma_f32_16x16x128_f8f6f4 v[12:15], v[0:7], v[170:177], v[248:251]
	v_mfma_f32_16x16x128_f8f6f4 v[8:11], v[16:23], v[170:177], v[186:189]
	s_setprio 0
	s_setprio 1
	v_mfma_f32_16x16x128_f8f6f4 v[52:55], v[138:145], v[32:39], v[52:55]
	v_mfma_f32_16x16x128_f8f6f4 v[48:51], v[146:153], v[32:39], v[48:51]
	v_mfma_f32_16x16x128_f8f6f4 v[36:39], v[138:145], v[154:161], v[190:193]
	v_mfma_f32_16x16x128_f8f6f4 v[32:35], v[146:153], v[154:161], v[210:213]
	v_mfma_f32_16x16x128_f8f6f4 v[20:23], v[138:145], v[162:169], v[206:209]
	v_mfma_f32_16x16x128_f8f6f4 v[16:19], v[146:153], v[162:169], v[214:217]
	v_mfma_f32_16x16x128_f8f6f4 v[4:7], v[138:145], v[170:177], v[222:225]
	v_mfma_f32_16x16x128_f8f6f4 v[0:3], v[146:153], v[170:177], v[218:221]
	s_setprio 0
	s_barrier
	s_add_i32 s28, s28, 2
	s_add_u32 s22, s22, 0x100
	s_addc_u32 s23, s23, 0
	s_add_u32 s17, s17, 0x100
	s_addc_u32 s19, s19, 0

.LBB0_750:
	s_ashr_i32 s19, s18, 31
	s_lshl_b64 s[20:21], s[18:19], 18
	s_add_u32 s20, s33, s20
	s_addc_u32 s21, s34, s21
	s_and_b64 s[22:23], s[2:3], exec
	s_cselect_b32 s5, s21, s27
	s_cselect_b32 s19, s20, s26
	s_ashr_i32 s17, s16, 31
	s_lshl_b64 s[22:23], s[16:17], 18
	s_add_u32 s22, s35, s22
	s_addc_u32 s23, s36, s23
	s_and_b64 s[30:31], s[2:3], exec
	s_cselect_b32 s17, s23, s29
	s_cselect_b32 s25, s22, s28
	s_add_u32 s26, s26, 0x20080
	s_addc_u32 s27, s27, 0
	s_add_u32 s68, s28, 0x100
	v_mov_b32_e32 v183, 0x1200
	s_addc_u32 s70, s29, 0
	s_mov_b32 s72, -2
	ds_read_b128 v[128:131], v162
	ds_read_b128 v[136:139], v162 offset:2048
	ds_read_b128 v[132:135], v163
	ds_read_b128 v[140:143], v163 offset:2048
	ds_read_b128 v[144:147], v162 offset:16384
	ds_read_b128 v[152:155], v162 offset:18432
	ds_read_b128 v[148:151], v163 offset:16384
	ds_read_b128 v[156:159], v163 offset:18432
	s_add_u32 s28, s26, 0xfffe0080
	s_addc_u32 s29, s27, -1
	s_cmp_eq_u32 s72, 4
	s_cselect_b32 s29, s5, s29
	s_cselect_b32 s28, s19, s28
	s_cselect_b32 s31, s17, s70
	s_cselect_b32 s30, s25, s68
	v_mov_b32_e32 v182, v164
	ds_read_b128 v[166:169], v160
	ds_read_b128 v[174:177], v160 offset:2048
	ds_read_b128 v[170:173], v161
	ds_read_b128 v[178:181], v161 offset:2048
	ds_read_b128 v[194:197], v160 offset:4096
	ds_read_b128 v[228:231], v160 offset:6144
	ds_read_b128 v[198:201], v161 offset:4096
	ds_read_b128 v[232:235], v161 offset:6144
	s_add_i32 m0, s37, 0xc000
	s_nop 0
	global_load_lds_dwordx4 v182, s[26:27]
	v_mov_b32_e32 v182, v165
	s_add_i32 m0, s37, 0xe000
	s_nop 0
	global_load_lds_dwordx4 v182, s[26:27]
	s_waitcnt vmcnt(8)
	s_waitcnt lgkmcnt(0)
	s_barrier
	s_setprio 1
	s_waitcnt lgkmcnt(0)
	v_mfma_f32_16x16x128_f8f6f4 v[124:127], v[128:135], v[166:173], 0
	v_mfma_f32_16x16x128_f8f6f4 v[120:123], v[136:143], v[166:173], 0
	v_mfma_f32_16x16x128_f8f6f4 v[108:111], v[128:135], v[174:181], 0
	v_mfma_f32_16x16x128_f8f6f4 v[104:107], v[136:143], v[174:181], 0
	v_mfma_f32_16x16x128_f8f6f4 v[186:189], v[128:135], v[194:201], 0
	v_mfma_f32_16x16x128_f8f6f4 v[190:193], v[136:143], v[194:201], 0
	v_mfma_f32_16x16x128_f8f6f4 v[202:205], v[128:135], v[228:235], 0
	v_mfma_f32_16x16x128_f8f6f4 v[206:209], v[136:143], v[228:235], 0
	s_setprio 0
	s_setprio 1
	v_mfma_f32_16x16x128_f8f6f4 v[116:119], v[144:151], v[166:173], 0
	v_mfma_f32_16x16x128_f8f6f4 v[112:115], v[152:159], v[166:173], 0
	v_mfma_f32_16x16x128_f8f6f4 v[100:103], v[144:151], v[174:181], 0
	v_mfma_f32_16x16x128_f8f6f4 v[96:99], v[152:159], v[174:181], 0
	v_mfma_f32_16x16x128_f8f6f4 v[166:169], v[144:151], v[194:201], 0
	v_mfma_f32_16x16x128_f8f6f4 v[170:173], v[152:159], v[194:201], 0
	v_mfma_f32_16x16x128_f8f6f4 v[174:177], v[144:151], v[228:235], 0
	v_mfma_f32_16x16x128_f8f6f4 v[178:181], v[152:159], v[228:235], 0
	s_setprio 0
	s_barrier
	v_mov_b32_e32 v182, v164
	s_mov_b32 m0, s38
	s_nop 2
	ds_read_b128 v[64:67], v160 offset:16384
	ds_read_b128 v[72:75], v160 offset:18432
	ds_read_b128 v[68:71], v161 offset:16384
	ds_read_b128 v[76:79], v161 offset:18432
	ds_read_b128 v[80:83], v160 offset:20480
	ds_read_b128 v[88:91], v160 offset:22528
	ds_read_b128 v[84:87], v161 offset:20480
	ds_read_b128 v[92:95], v161 offset:22528
	s_add_u32 s74, s30, 0x20000
	global_load_lds_dwordx4 v182, s[30:31]
	v_mov_b32_e32 v182, v165
	s_mov_b32 m0, s39
	s_addc_u32 s75, s31, 0
	global_load_lds_dwordx4 v182, s[30:31]
	v_mov_b32_e32 v182, v164
	s_mov_b32 m0, s40
	s_nop 0
	global_load_lds_dwordx4 v182, s[74:75]
	v_mov_b32_e32 v182, v165
	s_mov_b32 m0, s42
	s_nop 0
	global_load_lds_dwordx4 v182, s[74:75]
	v_mov_b32_e32 v182, v164
	s_mov_b32 m0, s37
	s_nop 0
	global_load_lds_dwordx4 v182, s[28:29]
	v_mov_b32_e32 v182, v165
	s_mov_b32 m0, s43
	s_nop 0
	global_load_lds_dwordx4 v182, s[28:29]
	s_waitcnt vmcnt(8)
	s_waitcnt lgkmcnt(0)
	s_barrier
	s_setprio 1
	s_waitcnt lgkmcnt(0)
	v_mfma_f32_16x16x128_f8f6f4 v[60:63], v[128:135], v[64:71], 0
	v_mfma_f32_16x16x128_f8f6f4 v[56:59], v[136:143], v[64:71], 0
	v_mfma_f32_16x16x128_f8f6f4 v[194:197], v[128:135], v[72:79], 0
	v_mfma_f32_16x16x128_f8f6f4 v[198:201], v[136:143], v[72:79], 0
	v_mfma_f32_16x16x128_f8f6f4 v[210:213], v[128:135], v[80:87], 0
	v_mfma_f32_16x16x128_f8f6f4 v[214:217], v[136:143], v[80:87], 0
	v_mfma_f32_16x16x128_f8f6f4 v[218:221], v[128:135], v[88:95], 0
	v_mfma_f32_16x16x128_f8f6f4 v[222:225], v[136:143], v[88:95], 0
	s_setprio 0
	s_setprio 1
	v_mfma_f32_16x16x128_f8f6f4 v[52:55], v[144:151], v[64:71], 0
	v_mfma_f32_16x16x128_f8f6f4 v[48:51], v[152:159], v[64:71], 0
	v_mfma_f32_16x16x128_f8f6f4 v[228:231], v[144:151], v[72:79], 0
	v_mfma_f32_16x16x128_f8f6f4 v[232:235], v[152:159], v[72:79], 0
	v_mfma_f32_16x16x128_f8f6f4 v[236:239], v[144:151], v[80:87], 0
	v_mfma_f32_16x16x128_f8f6f4 v[240:243], v[152:159], v[80:87], 0
	v_mfma_f32_16x16x128_f8f6f4 v[244:247], v[144:151], v[88:95], 0
	v_mfma_f32_16x16x128_f8f6f4 v[248:251], v[152:159], v[88:95], 0
	s_setprio 0
	s_barrier
	s_nop 4
	ds_read_b128 v[0:3], v162 offset:32768
	ds_read_b128 v[16:19], v162 offset:34816
	ds_read_b128 v[4:7], v163 offset:32768
	ds_read_b128 v[20:23], v163 offset:34816
	ds_read_b128 v[128:131], v162 offset:49152
	ds_read_b128 v[136:139], v162 offset:51200
	ds_read_b128 v[132:135], v163 offset:49152
	ds_read_b128 v[140:143], v163 offset:51200
	s_add_u32 s74, s28, 0x20000
	v_mov_b32_e32 v64, v164
	s_mov_b32 m0, s44
	ds_read_b128 v[8:11], v160 offset:32768
	ds_read_b128 v[24:27], v160 offset:34816
	ds_read_b128 v[12:15], v161 offset:32768
	ds_read_b128 v[28:31], v161 offset:34816
	ds_read_b128 v[32:35], v160 offset:36864
	ds_read_b128 v[40:43], v160 offset:38912
	ds_read_b128 v[36:39], v161 offset:36864
	ds_read_b128 v[44:47], v161 offset:38912
	s_addc_u32 s75, s29, 0
	s_nop 0
	global_load_lds_dwordx4 v64, s[74:75]
	v_mov_b32_e32 v64, v165
	s_mov_b32 m0, s49
	s_nop 0
	global_load_lds_dwordx4 v64, s[74:75]
	s_waitcnt vmcnt(8)
	s_waitcnt lgkmcnt(0)
	s_barrier
	s_setprio 1
	s_waitcnt lgkmcnt(0)
	v_mfma_f32_16x16x128_f8f6f4 v[124:127], v[0:7], v[8:15], v[124:127]
	v_mfma_f32_16x16x128_f8f6f4 v[120:123], v[16:23], v[8:15], v[120:123]
	v_mfma_f32_16x16x128_f8f6f4 v[108:111], v[0:7], v[24:31], v[108:111]
	v_mfma_f32_16x16x128_f8f6f4 v[104:107], v[16:23], v[24:31], v[104:107]
	v_mfma_f32_16x16x128_f8f6f4 v[92:95], v[0:7], v[32:39], v[186:189]
	v_mfma_f32_16x16x128_f8f6f4 v[88:91], v[16:23], v[32:39], v[190:193]
	v_mfma_f32_16x16x128_f8f6f4 v[76:79], v[0:7], v[40:47], v[202:205]
	v_mfma_f32_16x16x128_f8f6f4 v[72:75], v[16:23], v[40:47], v[206:209]
	s_setprio 0
	s_setprio 1
	v_mfma_f32_16x16x128_f8f6f4 v[116:119], v[128:135], v[8:15], v[116:119]
	v_mfma_f32_16x16x128_f8f6f4 v[112:115], v[136:143], v[8:15], v[112:115]
	v_mfma_f32_16x16x128_f8f6f4 v[100:103], v[128:135], v[24:31], v[100:103]
	v_mfma_f32_16x16x128_f8f6f4 v[96:99], v[136:143], v[24:31], v[96:99]
	v_mfma_f32_16x16x128_f8f6f4 v[84:87], v[128:135], v[32:39], v[166:169]
	v_mfma_f32_16x16x128_f8f6f4 v[80:83], v[136:143], v[32:39], v[170:173]
	v_mfma_f32_16x16x128_f8f6f4 v[68:71], v[128:135], v[40:47], v[174:177]
	v_mfma_f32_16x16x128_f8f6f4 v[64:67], v[136:143], v[40:47], v[178:181]
	s_setprio 0
	s_barrier
	v_mov_b32_e32 v184, v164
	ds_read_b128 v[32:35], v160 offset:49152
	ds_read_b128 v[144:147], v160 offset:51200
	ds_read_b128 v[36:39], v161 offset:49152
	ds_read_b128 v[148:151], v161 offset:51200
	ds_read_b128 v[152:155], v160 offset:53248
	ds_read_b128 v[166:169], v160 offset:55296
	ds_read_b128 v[156:159], v161 offset:53248
	ds_read_b128 v[170:173], v161 offset:55296
	s_mov_b32 m0, s54
	v_lshl_add_u64 v[8:9], s[30:31], 0, v[184:185]
	v_lshl_add_u64 v[8:9], v[8:9], 0, s[46:47]
	v_mov_b32_e32 v184, v165
	global_load_lds_dwordx4 v[8:9], off
	s_mov_b32 m0, s55
	v_lshl_add_u64 v[8:9], s[30:31], 0, v[184:185]
	v_lshl_add_u64 v[8:9], v[8:9], 0, s[46:47]
	global_load_lds_dwordx4 v[8:9], off
	s_add_u32 s30, s30, 0x20080
	v_mov_b32_e32 v8, v164
	s_addc_u32 s31, s31, 0
	s_mov_b32 m0, s59
	v_mov_b32_e32 v184, v164
	global_load_lds_dwordx4 v8, s[30:31]
	v_mov_b32_e32 v8, v165
	s_mov_b32 m0, s64
	s_nop 0
	global_load_lds_dwordx4 v8, s[30:31]
	s_mov_b32 m0, s56
	v_lshl_add_u64 v[8:9], s[28:29], 0, v[184:185]
	v_lshl_add_u64 v[8:9], v[8:9], 0, s[46:47]
	v_mov_b32_e32 v184, v165
	global_load_lds_dwordx4 v[8:9], off
	s_mov_b32 m0, s57
	v_lshl_add_u64 v[8:9], s[28:29], 0, v[184:185]
	v_lshl_add_u64 v[8:9], v[8:9], 0, s[46:47]
	global_load_lds_dwordx4 v[8:9], off
	s_waitcnt vmcnt(8)
	s_waitcnt lgkmcnt(0)
	s_barrier
	s_setprio 1
	s_waitcnt lgkmcnt(0)
	v_mfma_f32_16x16x128_f8f6f4 v[60:63], v[0:7], v[32:39], v[60:63]
	v_mfma_f32_16x16x128_f8f6f4 v[56:59], v[16:23], v[32:39], v[56:59]
	v_mfma_f32_16x16x128_f8f6f4 v[44:47], v[0:7], v[144:151], v[194:197]
	v_mfma_f32_16x16x128_f8f6f4 v[40:43], v[16:23], v[144:151], v[198:201]
	v_mfma_f32_16x16x128_f8f6f4 v[28:31], v[0:7], v[152:159], v[210:213]
	v_mfma_f32_16x16x128_f8f6f4 v[24:27], v[16:23], v[152:159], v[214:217]
	v_mfma_f32_16x16x128_f8f6f4 v[12:15], v[0:7], v[166:173], v[218:221]
	v_mfma_f32_16x16x128_f8f6f4 v[8:11], v[16:23], v[166:173], v[222:225]
	s_setprio 0
	s_setprio 1
	v_mfma_f32_16x16x128_f8f6f4 v[52:55], v[128:135], v[32:39], v[52:55]
	v_mfma_f32_16x16x128_f8f6f4 v[48:51], v[136:143], v[32:39], v[48:51]
	v_mfma_f32_16x16x128_f8f6f4 v[36:39], v[128:135], v[144:151], v[228:231]
	v_mfma_f32_16x16x128_f8f6f4 v[32:35], v[136:143], v[144:151], v[232:235]
	v_mfma_f32_16x16x128_f8f6f4 v[20:23], v[128:135], v[152:159], v[236:239]
	v_mfma_f32_16x16x128_f8f6f4 v[16:19], v[136:143], v[152:159], v[240:243]
	v_mfma_f32_16x16x128_f8f6f4 v[4:7], v[128:135], v[166:173], v[244:247]
	v_mfma_f32_16x16x128_f8f6f4 v[0:3], v[136:143], v[166:173], v[248:251]
	s_setprio 0
	s_barrier
	s_add_i32 s72, s72, 2
	s_add_u32 s26, s26, 0x100
	s_addc_u32 s27, s27, 0
	s_add_u32 s68, s68, 0x100
	s_addc_u32 s70, s70, 0

.LBB0_1034:
	v_readfirstlane_b32 s19, v4
	s_xor_b32 s27, s75, s19
	s_lshl_b32 s19, s75, 12
	s_add_i32 s74, s19, 0
	s_add_i32 s74, s74, 0x21000
	s_add_u32 s19, s24, 0x100
	s_addc_u32 s76, s25, 0
	s_mov_b32 s77, -2
	s_mov_b64 s[24:25], s[14:15]
	ds_read_b128 v[136:139], v150
	s_waitcnt vmcnt(0)
	ds_read_b128 v[156:159], v150 offset:2048
	ds_read_b128 v[140:143], v151
	ds_read_b128 v[160:163], v151 offset:2048
	ds_read_b128 v[164:167], v150 offset:16384
	ds_read_b128 v[172:175], v150 offset:18432
	ds_read_b128 v[168:171], v151 offset:16384
	ds_read_b128 v[176:179], v151 offset:18432
	s_add_u32 s28, s24, 0x80
	s_addc_u32 s29, s25, 0
	s_cmp_eq_u32 s77, 4
	s_cselect_b32 s29, s11, s29
	s_cselect_b32 s28, s10, s28
	s_cselect_b32 s80, s27, s75
	s_cselect_b32 s37, s23, s76
	s_cselect_b32 s36, s22, s19
	ds_read_b128 v[194:197], v148
	ds_read_b128 v[228:231], v148 offset:2048
	ds_read_b128 v[198:201], v149
	ds_read_b128 v[232:235], v149 offset:2048
	ds_read_b128 v[236:239], v148 offset:4096
	ds_read_b128 v[244:247], v148 offset:6144
	ds_read_b128 v[240:243], v149 offset:4096
	ds_read_b128 v[248:251], v149 offset:6144
	v_mbcnt_lo_u32_b32 v40, -1, 0
	v_mbcnt_hi_u32_b32 v40, -1, v40
	s_mov_b32 s78, s61
	v_lshlrev_b32_e32 v40, 3, v40
	s_add_i32 m0, s35, 0xc000
	v_lshl_or_b32 v40, s78, 9, v40
	v_add_u32_e32 v40, s74, v40
	ds_read_b32 v40, v40 offset:4
	s_waitcnt lgkmcnt(0)
	v_lshlrev_b32_e32 v41, 10, v40
	v_and_or_b32 v41, v41, s69, v154
	v_bfe_u32 v40, v40, 16, 16
	v_lshl_or_b32 v40, v40, 10, v154
	global_load_lds_dwordx4 v41, s[24:25]
	s_add_i32 m0, s35, 0xe000
	s_nop 0
	global_load_lds_dwordx4 v40, s[24:25]
	s_waitcnt vmcnt(8)
	s_waitcnt lgkmcnt(0)
	s_barrier
	s_setprio 1
	v_mfma_f32_16x16x128_f8f6f4 v[132:135], v[136:143], v[194:201], 0
	v_mfma_f32_16x16x128_f8f6f4 v[124:127], v[156:163], v[194:201], 0
	v_mfma_f32_16x16x128_f8f6f4 v[116:119], v[136:143], v[228:235], 0
	v_mfma_f32_16x16x128_f8f6f4 v[108:111], v[156:163], v[228:235], 0
	v_mfma_f32_16x16x128_f8f6f4 v[144:147], v[136:143], v[236:243], 0
	v_mfma_f32_16x16x128_f8f6f4 v[180:183], v[156:163], v[236:243], 0
	v_mfma_f32_16x16x128_f8f6f4 v[186:189], v[136:143], v[244:251], 0
	v_mfma_f32_16x16x128_f8f6f4 v[190:193], v[156:163], v[244:251], 0
	s_setprio 0
	s_setprio 1
	v_mfma_f32_16x16x128_f8f6f4 v[128:131], v[164:171], v[194:201], 0
	v_mfma_f32_16x16x128_f8f6f4 v[120:123], v[172:179], v[194:201], 0
	v_mfma_f32_16x16x128_f8f6f4 v[112:115], v[164:171], v[228:235], 0
	v_mfma_f32_16x16x128_f8f6f4 v[104:107], v[172:179], v[228:235], 0
	v_mfma_f32_16x16x128_f8f6f4 v[202:205], v[164:171], v[236:243], 0
	v_mfma_f32_16x16x128_f8f6f4 v[206:209], v[172:179], v[236:243], 0
	v_mfma_f32_16x16x128_f8f6f4 v[210:213], v[164:171], v[244:251], 0
	v_mfma_f32_16x16x128_f8f6f4 v[214:217], v[172:179], v[244:251], 0
	s_setprio 0
	s_barrier
	v_mov_b32_e32 v40, v152
	s_mov_b32 m0, s44
	s_nop 2
	ds_read_b128 v[72:75], v148 offset:16384
	ds_read_b128 v[80:83], v148 offset:18432
	ds_read_b128 v[76:79], v149 offset:16384
	ds_read_b128 v[84:87], v149 offset:18432
	ds_read_b128 v[88:91], v148 offset:20480
	ds_read_b128 v[96:99], v148 offset:22528
	ds_read_b128 v[92:95], v149 offset:20480
	ds_read_b128 v[100:103], v149 offset:22528
	s_add_u32 s78, s36, 0x20000
	global_load_lds_dwordx4 v40, s[36:37]
	v_mov_b32_e32 v40, v153
	s_mov_b32 m0, s49
	s_addc_u32 s79, s37, 0
	global_load_lds_dwordx4 v40, s[36:37]
	v_mov_b32_e32 v40, v152
	s_mov_b32 m0, s50
	s_nop 0
	global_load_lds_dwordx4 v40, s[78:79]
	v_mov_b32_e32 v40, v153
	s_mov_b32 m0, s51
	s_nop 0
	global_load_lds_dwordx4 v40, s[78:79]
	v_mbcnt_lo_u32_b32 v40, -1, 0
	v_mbcnt_hi_u32_b32 v40, -1, v40
	s_mov_b32 s78, s61
	v_lshlrev_b32_e32 v40, 3, v40
	v_lshl_or_b32 v40, s78, 9, v40
	s_lshl_b32 s78, s80, 12
	s_add_i32 s78, s78, 0
	s_add_i32 s78, s78, 0x21000
	v_add_u32_e32 v40, s78, v40
	ds_read_b32 v40, v40
	s_mov_b32 m0, s35
	s_waitcnt lgkmcnt(0)
	v_lshlrev_b32_e32 v41, 10, v40
	v_and_or_b32 v41, v41, s69, v154
	v_bfe_u32 v40, v40, 16, 16
	v_lshl_or_b32 v40, v40, 10, v154
	global_load_lds_dwordx4 v41, s[28:29]
	s_mov_b32 m0, s54
	s_nop 0
	global_load_lds_dwordx4 v40, s[28:29]
	s_waitcnt vmcnt(8)
	s_waitcnt lgkmcnt(0)
	s_barrier
	s_setprio 1
	v_mfma_f32_16x16x128_f8f6f4 v[48:51], v[136:143], v[80:87], 0
	v_mfma_f32_16x16x128_f8f6f4 v[36:39], v[156:163], v[80:87], 0
	v_mfma_f32_16x16x128_f8f6f4 v[28:31], v[136:143], v[88:95], 0
	v_mfma_f32_16x16x128_f8f6f4 v[20:23], v[156:163], v[88:95], 0
	v_mfma_f32_16x16x128_f8f6f4 v[12:15], v[136:143], v[96:103], 0
	v_mfma_f32_16x16x128_f8f6f4 v[4:7], v[156:163], v[96:103], 0
	v_mfma_f32_16x16x128_f8f6f4 v[40:43], v[136:143], v[72:79], 0
	v_mfma_f32_16x16x128_f8f6f4 v[52:55], v[156:163], v[72:79], 0
	s_setprio 0
	s_setprio 1
	v_mfma_f32_16x16x128_f8f6f4 v[64:67], v[164:171], v[72:79], 0
	v_mfma_f32_16x16x128_f8f6f4 v[56:59], v[172:179], v[72:79], 0
	v_mfma_f32_16x16x128_f8f6f4 v[44:47], v[164:171], v[80:87], 0
	v_mfma_f32_16x16x128_f8f6f4 v[32:35], v[172:179], v[80:87], 0
	v_mfma_f32_16x16x128_f8f6f4 v[24:27], v[164:171], v[88:95], 0
	v_mfma_f32_16x16x128_f8f6f4 v[16:19], v[172:179], v[88:95], 0
	v_mfma_f32_16x16x128_f8f6f4 v[8:11], v[164:171], v[96:103], 0
	v_mfma_f32_16x16x128_f8f6f4 v[0:3], v[172:179], v[96:103], 0
	s_setprio 0
	s_barrier
	ds_read_b128 v[136:139], v150 offset:32768
	ds_read_b128 v[156:159], v150 offset:34816
	ds_read_b128 v[140:143], v151 offset:32768
	ds_read_b128 v[160:163], v151 offset:34816
	ds_read_b128 v[164:167], v150 offset:49152
	ds_read_b128 v[172:175], v150 offset:51200
	ds_read_b128 v[168:171], v151 offset:49152
	ds_read_b128 v[176:179], v151 offset:51200
	ds_read_b128 v[68:71], v148 offset:32768
	ds_read_b128 v[194:197], v148 offset:34816
	ds_read_b128 v[72:75], v149 offset:32768
	ds_read_b128 v[198:201], v149 offset:34816
	ds_read_b128 v[228:231], v148 offset:36864
	ds_read_b128 v[236:239], v148 offset:38912
	ds_read_b128 v[232:235], v149 offset:36864
	ds_read_b128 v[240:243], v149 offset:38912
	v_mbcnt_lo_u32_b32 v60, -1, 0
	v_mbcnt_hi_u32_b32 v60, -1, v60
	s_mov_b32 s79, s61
	v_lshlrev_b32_e32 v60, 3, v60
	s_mov_b32 m0, s55
	v_lshl_or_b32 v60, s79, 9, v60
	v_add_u32_e32 v60, s78, v60
	ds_read_b32 v60, v60 offset:4
	s_waitcnt lgkmcnt(0)
	v_lshlrev_b32_e32 v61, 10, v60
	v_and_or_b32 v61, v61, s69, v154
	v_bfe_u32 v60, v60, 16, 16
	v_lshl_or_b32 v60, v60, 10, v154
	global_load_lds_dwordx4 v61, s[28:29]
	s_mov_b32 m0, s56
	s_nop 0
	global_load_lds_dwordx4 v60, s[28:29]
	s_waitcnt vmcnt(8)
	s_waitcnt lgkmcnt(0)
	s_barrier
	s_setprio 1
	v_mfma_f32_16x16x128_f8f6f4 v[132:135], v[136:143], v[68:75], v[132:135]
	v_mfma_f32_16x16x128_f8f6f4 v[124:127], v[156:163], v[68:75], v[124:127]
	v_mfma_f32_16x16x128_f8f6f4 v[116:119], v[136:143], v[194:201], v[116:119]
	v_mfma_f32_16x16x128_f8f6f4 v[108:111], v[156:163], v[194:201], v[108:111]
	v_mfma_f32_16x16x128_f8f6f4 v[100:103], v[136:143], v[228:235], v[144:147]
	v_mfma_f32_16x16x128_f8f6f4 v[92:95], v[156:163], v[228:235], v[180:183]
	v_mfma_f32_16x16x128_f8f6f4 v[84:87], v[136:143], v[236:243], v[186:189]
	v_mfma_f32_16x16x128_f8f6f4 v[76:79], v[156:163], v[236:243], v[190:193]
	s_setprio 0
	s_setprio 1
	v_mfma_f32_16x16x128_f8f6f4 v[128:131], v[164:171], v[68:75], v[128:131]
	v_mfma_f32_16x16x128_f8f6f4 v[120:123], v[172:179], v[68:75], v[120:123]
	v_mfma_f32_16x16x128_f8f6f4 v[112:115], v[164:171], v[194:201], v[112:115]
	v_mfma_f32_16x16x128_f8f6f4 v[104:107], v[172:179], v[194:201], v[104:107]
	v_mfma_f32_16x16x128_f8f6f4 v[96:99], v[164:171], v[228:235], v[202:205]
	v_mfma_f32_16x16x128_f8f6f4 v[88:91], v[172:179], v[228:235], v[206:209]
	v_mfma_f32_16x16x128_f8f6f4 v[80:83], v[164:171], v[236:243], v[210:213]
	v_mfma_f32_16x16x128_f8f6f4 v[72:75], v[172:179], v[236:243], v[214:217]
	s_setprio 0
	s_barrier
	v_mov_b32_e32 v184, v152
	ds_read_b128 v[194:197], v148 offset:49152
	ds_read_b128 v[228:231], v148 offset:51200
	ds_read_b128 v[198:201], v149 offset:49152
	ds_read_b128 v[232:235], v149 offset:51200
	ds_read_b128 v[236:239], v148 offset:53248
	ds_read_b128 v[244:247], v148 offset:55296
	ds_read_b128 v[240:243], v149 offset:53248
	ds_read_b128 v[248:251], v149 offset:55296
	s_mov_b32 m0, s57
	v_lshl_add_u64 v[60:61], s[36:37], 0, v[184:185]
	v_lshl_add_u64 v[60:61], v[60:61], 0, s[46:47]
	v_mov_b32_e32 v184, v153
	global_load_lds_dwordx4 v[60:61], off
	s_mov_b32 m0, s59
	v_lshl_add_u64 v[60:61], s[36:37], 0, v[184:185]
	v_lshl_add_u64 v[60:61], v[60:61], 0, s[46:47]
	global_load_lds_dwordx4 v[60:61], off
	s_add_u32 s36, s36, 0x20080
	v_mov_b32_e32 v60, v152
	s_addc_u32 s37, s37, 0
	s_mov_b32 m0, s66
	s_nop 0
	global_load_lds_dwordx4 v60, s[36:37]
	v_mov_b32_e32 v60, v153
	s_mov_b32 m0, s67
	s_nop 0
	global_load_lds_dwordx4 v60, s[36:37]
	v_mbcnt_lo_u32_b32 v60, -1, 0
	v_mbcnt_hi_u32_b32 v60, -1, v60
	s_mov_b32 s36, s61
	v_lshlrev_b32_e32 v60, 3, v60
	s_mov_b32 m0, s64
	v_lshl_or_b32 v60, s36, 9, v60
	v_add_u32_e32 v60, s78, v60
	ds_read_b32 v62, v60
	s_waitcnt lgkmcnt(0)
	v_lshlrev_b32_e32 v60, 10, v62
	v_and_or_b32 v184, v60, s69, v154
	s_nop 0
	v_lshl_add_u64 v[60:61], s[28:29], 0, v[184:185]
	v_lshl_add_u64 v[60:61], v[60:61], 0, s[46:47]
	global_load_lds_dwordx4 v[60:61], off
	v_bfe_u32 v60, v62, 16, 16
	v_lshl_or_b32 v184, v60, 10, v154
	s_mov_b32 m0, s65
	v_lshl_add_u64 v[60:61], s[28:29], 0, v[184:185]
	v_lshl_add_u64 v[60:61], v[60:61], 0, s[46:47]
	global_load_lds_dwordx4 v[60:61], off
	s_waitcnt vmcnt(8)
	s_waitcnt lgkmcnt(0)
	s_barrier
	s_setprio 1
	v_mfma_f32_16x16x128_f8f6f4 v[68:71], v[136:143], v[194:201], v[40:43]
	v_mfma_f32_16x16x128_f8f6f4 v[60:63], v[156:163], v[194:201], v[52:55]
	v_mfma_f32_16x16x128_f8f6f4 v[48:51], v[136:143], v[228:235], v[48:51]
	v_mfma_f32_16x16x128_f8f6f4 v[36:39], v[156:163], v[228:235], v[36:39]
	v_mfma_f32_16x16x128_f8f6f4 v[28:31], v[136:143], v[236:243], v[28:31]
	v_mfma_f32_16x16x128_f8f6f4 v[20:23], v[156:163], v[236:243], v[20:23]
	v_mfma_f32_16x16x128_f8f6f4 v[12:15], v[136:143], v[244:251], v[12:15]
	v_mfma_f32_16x16x128_f8f6f4 v[4:7], v[156:163], v[244:251], v[4:7]
	s_setprio 0
	s_setprio 1
	v_mfma_f32_16x16x128_f8f6f4 v[64:67], v[164:171], v[194:201], v[64:67]
	v_mfma_f32_16x16x128_f8f6f4 v[56:59], v[172:179], v[194:201], v[56:59]
	v_mfma_f32_16x16x128_f8f6f4 v[44:47], v[164:171], v[228:235], v[44:47]
	v_mfma_f32_16x16x128_f8f6f4 v[32:35], v[172:179], v[228:235], v[32:35]
	v_mfma_f32_16x16x128_f8f6f4 v[24:27], v[164:171], v[236:243], v[24:27]
	v_mfma_f32_16x16x128_f8f6f4 v[16:19], v[172:179], v[236:243], v[16:19]
	v_mfma_f32_16x16x128_f8f6f4 v[8:11], v[164:171], v[244:251], v[8:11]
	v_mfma_f32_16x16x128_f8f6f4 v[0:3], v[172:179], v[244:251], v[0:3]
	s_setprio 0
	s_barrier
	s_add_i32 s77, s77, 2
	s_add_u32 s24, s24, 0x100
	s_addc_u32 s25, s25, 0
	s_add_u32 s19, s19, 0x100
	s_addc_u32 s76, s76, 0

.LBB0_1113:
	s_ashr_i32 s25, s24, 31
	s_lshl_b64 s[22:23], s[24:25], 18
	s_add_u32 s22, s38, s22
	s_addc_u32 s23, s39, s23
	s_and_b64 s[34:35], s[10:11], exec
	s_cselect_b32 s7, s23, s29
	s_cselect_b32 s21, s22, s28
	s_add_u32 s28, s28, 0x20080
	s_addc_u32 s29, s29, 0
	s_add_u32 s25, s30, 0x100
	s_addc_u32 s80, s31, 0
	s_mov_b32 s81, -2
	ds_read_b128 v[128:131], v148
	ds_read_b128 v[136:139], v148 offset:2048
	ds_read_b128 v[132:135], v149
	ds_read_b128 v[140:143], v149 offset:2048
	ds_read_b128 v[152:155], v148 offset:16384
	ds_read_b128 v[160:163], v148 offset:18432
	ds_read_b128 v[156:159], v149 offset:16384
	ds_read_b128 v[164:167], v149 offset:18432
	s_add_u32 s30, s28, 0xfffe0080
	s_addc_u32 s31, s29, -1
	s_cmp_eq_u32 s81, 4
	s_cselect_b32 s31, s7, s31
	s_cselect_b32 s30, s21, s30
	s_cselect_b32 s35, s19, s80
	s_cselect_b32 s34, s18, s25
	v_mov_b32_e32 v144, v150
	ds_read_b128 v[168:171], v146
	ds_read_b128 v[176:179], v146 offset:2048
	ds_read_b128 v[172:175], v147
	ds_read_b128 v[180:183], v147 offset:2048
	ds_read_b128 v[194:197], v146 offset:4096
	ds_read_b128 v[228:231], v146 offset:6144
	ds_read_b128 v[198:201], v147 offset:4096
	ds_read_b128 v[232:235], v147 offset:6144
	s_add_i32 m0, s27, 0xc000
	s_nop 0
	global_load_lds_dwordx4 v144, s[28:29]
	v_mov_b32_e32 v144, v151
	s_add_i32 m0, s27, 0xe000
	s_nop 0
	global_load_lds_dwordx4 v144, s[28:29]
	s_waitcnt vmcnt(8)
	s_waitcnt lgkmcnt(0)
	s_barrier
	s_setprio 1
	s_waitcnt lgkmcnt(0)
	v_mfma_f32_16x16x128_f8f6f4 v[124:127], v[128:135], v[168:175], 0
	v_mfma_f32_16x16x128_f8f6f4 v[120:123], v[136:143], v[168:175], 0
	v_mfma_f32_16x16x128_f8f6f4 v[108:111], v[128:135], v[176:183], 0
	v_mfma_f32_16x16x128_f8f6f4 v[104:107], v[136:143], v[176:183], 0
	v_mfma_f32_16x16x128_f8f6f4 v[186:189], v[128:135], v[194:201], 0
	v_mfma_f32_16x16x128_f8f6f4 v[190:193], v[136:143], v[194:201], 0
	v_mfma_f32_16x16x128_f8f6f4 v[202:205], v[128:135], v[228:235], 0
	v_mfma_f32_16x16x128_f8f6f4 v[206:209], v[136:143], v[228:235], 0
	s_setprio 0
	s_setprio 1
	v_mfma_f32_16x16x128_f8f6f4 v[116:119], v[152:159], v[168:175], 0
	v_mfma_f32_16x16x128_f8f6f4 v[112:115], v[160:167], v[168:175], 0
	v_mfma_f32_16x16x128_f8f6f4 v[100:103], v[152:159], v[176:183], 0
	v_mfma_f32_16x16x128_f8f6f4 v[96:99], v[160:167], v[176:183], 0
	v_mfma_f32_16x16x128_f8f6f4 v[168:171], v[152:159], v[194:201], 0
	v_mfma_f32_16x16x128_f8f6f4 v[172:175], v[160:167], v[194:201], 0
	v_mfma_f32_16x16x128_f8f6f4 v[176:179], v[152:159], v[228:235], 0
	v_mfma_f32_16x16x128_f8f6f4 v[180:183], v[160:167], v[228:235], 0
	s_setprio 0
	s_barrier
	v_mov_b32_e32 v144, v150
	s_mov_b32 m0, s43
	s_nop 2
	ds_read_b128 v[64:67], v146 offset:16384
	ds_read_b128 v[72:75], v146 offset:18432
	ds_read_b128 v[68:71], v147 offset:16384
	ds_read_b128 v[76:79], v147 offset:18432
	ds_read_b128 v[80:83], v146 offset:20480
	ds_read_b128 v[88:91], v146 offset:22528
	ds_read_b128 v[84:87], v147 offset:20480
	ds_read_b128 v[92:95], v147 offset:22528
	s_add_u32 s82, s34, 0x20000
	global_load_lds_dwordx4 v144, s[34:35]
	v_mov_b32_e32 v144, v151
	s_mov_b32 m0, s44
	s_addc_u32 s83, s35, 0
	global_load_lds_dwordx4 v144, s[34:35]
	v_mov_b32_e32 v144, v150
	s_mov_b32 m0, s49
	s_nop 0
	global_load_lds_dwordx4 v144, s[82:83]
	v_mov_b32_e32 v144, v151
	s_mov_b32 m0, s50
	s_nop 0
	global_load_lds_dwordx4 v144, s[82:83]
	v_mov_b32_e32 v144, v150
	s_mov_b32 m0, s27
	s_nop 0
	global_load_lds_dwordx4 v144, s[30:31]
	v_mov_b32_e32 v144, v151
	s_mov_b32 m0, s51
	s_nop 0
	global_load_lds_dwordx4 v144, s[30:31]
	s_waitcnt vmcnt(8)
	s_waitcnt lgkmcnt(0)
	s_barrier
	s_setprio 1
	s_waitcnt lgkmcnt(0)
	v_mfma_f32_16x16x128_f8f6f4 v[60:63], v[128:135], v[64:71], 0
	v_mfma_f32_16x16x128_f8f6f4 v[56:59], v[136:143], v[64:71], 0
	v_mfma_f32_16x16x128_f8f6f4 v[194:197], v[128:135], v[72:79], 0
	v_mfma_f32_16x16x128_f8f6f4 v[198:201], v[136:143], v[72:79], 0
	v_mfma_f32_16x16x128_f8f6f4 v[210:213], v[128:135], v[80:87], 0
	v_mfma_f32_16x16x128_f8f6f4 v[214:217], v[136:143], v[80:87], 0
	v_mfma_f32_16x16x128_f8f6f4 v[218:221], v[128:135], v[88:95], 0
	v_mfma_f32_16x16x128_f8f6f4 v[222:225], v[136:143], v[88:95], 0
	s_setprio 0
	s_setprio 1
	v_mfma_f32_16x16x128_f8f6f4 v[52:55], v[152:159], v[64:71], 0
	v_mfma_f32_16x16x128_f8f6f4 v[48:51], v[160:167], v[64:71], 0
	v_mfma_f32_16x16x128_f8f6f4 v[228:231], v[152:159], v[72:79], 0
	v_mfma_f32_16x16x128_f8f6f4 v[232:235], v[160:167], v[72:79], 0
	v_mfma_f32_16x16x128_f8f6f4 v[236:239], v[152:159], v[80:87], 0
	v_mfma_f32_16x16x128_f8f6f4 v[240:243], v[160:167], v[80:87], 0
	v_mfma_f32_16x16x128_f8f6f4 v[244:247], v[152:159], v[88:95], 0
	v_mfma_f32_16x16x128_f8f6f4 v[248:251], v[160:167], v[88:95], 0
	s_setprio 0
	s_barrier
	s_nop 4
	ds_read_b128 v[0:3], v148 offset:32768
	ds_read_b128 v[16:19], v148 offset:34816
	ds_read_b128 v[4:7], v149 offset:32768
	ds_read_b128 v[20:23], v149 offset:34816
	ds_read_b128 v[128:131], v148 offset:49152
	ds_read_b128 v[136:139], v148 offset:51200
	ds_read_b128 v[132:135], v149 offset:49152
	ds_read_b128 v[140:143], v149 offset:51200
	s_add_u32 s82, s30, 0x20000
	v_mov_b32_e32 v64, v150
	s_mov_b32 m0, s54
	ds_read_b128 v[8:11], v146 offset:32768
	ds_read_b128 v[24:27], v146 offset:34816
	ds_read_b128 v[12:15], v147 offset:32768
	ds_read_b128 v[28:31], v147 offset:34816
	ds_read_b128 v[32:35], v146 offset:36864
	ds_read_b128 v[40:43], v146 offset:38912
	ds_read_b128 v[36:39], v147 offset:36864
	ds_read_b128 v[44:47], v147 offset:38912
	s_addc_u32 s83, s31, 0
	s_nop 0
	global_load_lds_dwordx4 v64, s[82:83]
	v_mov_b32_e32 v64, v151
	s_mov_b32 m0, s55
	s_nop 0
	global_load_lds_dwordx4 v64, s[82:83]
	s_waitcnt vmcnt(8)
	s_waitcnt lgkmcnt(0)
	s_barrier
	s_setprio 1
	s_waitcnt lgkmcnt(0)
	v_mfma_f32_16x16x128_f8f6f4 v[124:127], v[0:7], v[8:15], v[124:127]
	v_mfma_f32_16x16x128_f8f6f4 v[120:123], v[16:23], v[8:15], v[120:123]
	v_mfma_f32_16x16x128_f8f6f4 v[108:111], v[0:7], v[24:31], v[108:111]
	v_mfma_f32_16x16x128_f8f6f4 v[104:107], v[16:23], v[24:31], v[104:107]
	v_mfma_f32_16x16x128_f8f6f4 v[92:95], v[0:7], v[32:39], v[186:189]
	v_mfma_f32_16x16x128_f8f6f4 v[88:91], v[16:23], v[32:39], v[190:193]
	v_mfma_f32_16x16x128_f8f6f4 v[76:79], v[0:7], v[40:47], v[202:205]
	v_mfma_f32_16x16x128_f8f6f4 v[72:75], v[16:23], v[40:47], v[206:209]
	s_setprio 0
	s_setprio 1
	v_mfma_f32_16x16x128_f8f6f4 v[116:119], v[128:135], v[8:15], v[116:119]
	v_mfma_f32_16x16x128_f8f6f4 v[112:115], v[136:143], v[8:15], v[112:115]
	v_mfma_f32_16x16x128_f8f6f4 v[100:103], v[128:135], v[24:31], v[100:103]
	v_mfma_f32_16x16x128_f8f6f4 v[96:99], v[136:143], v[24:31], v[96:99]
	v_mfma_f32_16x16x128_f8f6f4 v[84:87], v[128:135], v[32:39], v[168:171]
	v_mfma_f32_16x16x128_f8f6f4 v[80:83], v[136:143], v[32:39], v[172:175]
	v_mfma_f32_16x16x128_f8f6f4 v[68:71], v[128:135], v[40:47], v[176:179]
	v_mfma_f32_16x16x128_f8f6f4 v[64:67], v[136:143], v[40:47], v[180:183]
	s_setprio 0
	s_barrier
	v_mov_b32_e32 v184, v150
	ds_read_b128 v[32:35], v146 offset:49152
	ds_read_b128 v[152:155], v146 offset:51200
	ds_read_b128 v[36:39], v147 offset:49152
	ds_read_b128 v[156:159], v147 offset:51200
	ds_read_b128 v[160:163], v146 offset:53248
	ds_read_b128 v[168:171], v146 offset:55296
	ds_read_b128 v[164:167], v147 offset:53248
	ds_read_b128 v[172:175], v147 offset:55296
	s_mov_b32 m0, s56
	v_lshl_add_u64 v[8:9], s[34:35], 0, v[184:185]
	v_lshl_add_u64 v[8:9], v[8:9], 0, s[46:47]
	v_mov_b32_e32 v184, v151
	global_load_lds_dwordx4 v[8:9], off
	s_mov_b32 m0, s57
	v_lshl_add_u64 v[8:9], s[34:35], 0, v[184:185]
	v_lshl_add_u64 v[8:9], v[8:9], 0, s[46:47]
	global_load_lds_dwordx4 v[8:9], off
	s_add_u32 s34, s34, 0x20080
	v_mov_b32_e32 v8, v150
	s_addc_u32 s35, s35, 0
	s_mov_b32 m0, s65
	v_mov_b32_e32 v184, v150
	global_load_lds_dwordx4 v8, s[34:35]
	v_mov_b32_e32 v8, v151
	s_mov_b32 m0, s66
	s_nop 0
	global_load_lds_dwordx4 v8, s[34:35]
	s_mov_b32 m0, s59
	v_lshl_add_u64 v[8:9], s[30:31], 0, v[184:185]
	v_lshl_add_u64 v[8:9], v[8:9], 0, s[46:47]
	v_mov_b32_e32 v184, v151
	global_load_lds_dwordx4 v[8:9], off
	s_mov_b32 m0, s64
	v_lshl_add_u64 v[8:9], s[30:31], 0, v[184:185]
	v_lshl_add_u64 v[8:9], v[8:9], 0, s[46:47]
	global_load_lds_dwordx4 v[8:9], off
	s_waitcnt vmcnt(8)
	s_waitcnt lgkmcnt(0)
	s_barrier
	s_setprio 1
	s_waitcnt lgkmcnt(0)
	v_mfma_f32_16x16x128_f8f6f4 v[60:63], v[0:7], v[32:39], v[60:63]
	v_mfma_f32_16x16x128_f8f6f4 v[56:59], v[16:23], v[32:39], v[56:59]
	v_mfma_f32_16x16x128_f8f6f4 v[44:47], v[0:7], v[152:159], v[194:197]
	v_mfma_f32_16x16x128_f8f6f4 v[40:43], v[16:23], v[152:159], v[198:201]
	v_mfma_f32_16x16x128_f8f6f4 v[28:31], v[0:7], v[160:167], v[210:213]
	v_mfma_f32_16x16x128_f8f6f4 v[24:27], v[16:23], v[160:167], v[214:217]
	v_mfma_f32_16x16x128_f8f6f4 v[12:15], v[0:7], v[168:175], v[218:221]
	v_mfma_f32_16x16x128_f8f6f4 v[8:11], v[16:23], v[168:175], v[222:225]
	s_setprio 0
	s_setprio 1
	v_mfma_f32_16x16x128_f8f6f4 v[52:55], v[128:135], v[32:39], v[52:55]
	v_mfma_f32_16x16x128_f8f6f4 v[48:51], v[136:143], v[32:39], v[48:51]
	v_mfma_f32_16x16x128_f8f6f4 v[36:39], v[128:135], v[152:159], v[228:231]
	v_mfma_f32_16x16x128_f8f6f4 v[32:35], v[136:143], v[152:159], v[232:235]
	v_mfma_f32_16x16x128_f8f6f4 v[20:23], v[128:135], v[160:167], v[236:239]
	v_mfma_f32_16x16x128_f8f6f4 v[16:19], v[136:143], v[160:167], v[240:243]
	v_mfma_f32_16x16x128_f8f6f4 v[4:7], v[128:135], v[168:175], v[244:247]
	v_mfma_f32_16x16x128_f8f6f4 v[0:3], v[136:143], v[168:175], v[248:251]
	s_setprio 0
	s_barrier
	s_add_i32 s81, s81, 2
	s_add_u32 s28, s28, 0x100
	s_addc_u32 s29, s29, 0
	s_add_u32 s25, s25, 0x100
	s_addc_u32 s80, s80, 0
